# block selection: radix loop skipped when the query block has at most 16 valid blocks (all valid blocks are selected anyway)
# baseline (speedup 1.0000x reference)
; __device__ __forceinline__ void att_unit_mfma(KArgs args, int b, int qb, LAS unsigned char* lds, int wave0, int lane0, int tid0) {
;     ...
;               key[k] = ((bits_ ^ ((bits_ >> 31) ? 0xFFFFFFFFu : 0x80000000u)) & ~63u) | (unsigned)(63 - j); }
;           unsigned T = 0u;
; #pragma unroll 1
;     ...
; #pragma unroll
;               for (int k = 0; k < 8; ++k) c += key[k] >= cand ? 1 : 0;
;               c += __builtin_amdgcn_update_dpp(0, c, 0xB1, 0xf, 0xf, true);
;               c += __builtin_amdgcn_update_dpp(0, c, 0x4E, 0xf, 0xf, true);
;               c += __builtin_amdgcn_update_dpp(0, c, 0x141, 0xf, 0xf, true);
;               T = c >= NTOP ? cand : T; }
;           unsigned bits = 0u;
; #pragma unroll
;           for (int k = 0; k < 8; ++k) bits |= (key[k] >= T && 8 * e8 + k <= qb) ? (1u << k) : 0u;
.LBB0_606:
	s_or_b64 exec, exec, s[6:7]
	v_cmp_lt_i32_e32 vcc, -1, v26
	s_movk_i32 s0, 0xffc0
	s_nop 0
	v_cndmask_b32_e32 v5, -1, v215, vcc
	v_cmp_lt_i32_e32 vcc, -1, v21
	v_bitop3_b32 v5, v5, s0, v26 bitop3:0x48
	v_sub_u32_e32 v5, v5, v23
	v_cndmask_b32_e32 v6, -1, v215, vcc
	v_cmp_lt_i32_e32 vcc, -1, v20
	v_bitop3_b32 v6, v6, s0, v21 bitop3:0x48
	v_sub_u32_e32 v6, v6, v22
	v_cndmask_b32_e32 v7, -1, v215, vcc
	v_cmp_lt_i32_e32 vcc, -1, v17
	v_bitop3_b32 v7, v7, s0, v20 bitop3:0x48
	v_sub_u32_e32 v7, v7, v19
	v_cndmask_b32_e32 v8, -1, v215, vcc
	v_cmp_lt_i32_e32 vcc, -1, v16
	v_bitop3_b32 v8, v8, s0, v17 bitop3:0x48
	v_sub_u32_e32 v8, v8, v18
	v_cndmask_b32_e32 v11, -1, v215, vcc
	v_cmp_lt_i32_e32 vcc, -1, v4
	v_bitop3_b32 v11, v11, s0, v16 bitop3:0x48
	v_sub_u32_e32 v11, v11, v13
	v_cndmask_b32_e32 v12, -1, v215, vcc
	v_bitop3_b32 v4, v12, s0, v4 bitop3:0x48
	v_sub_u32_e32 v4, v4, v10
	v_cmp_lt_i32_e32 vcc, -1, v9
	v_add_u32_e32 v10, 63, v4
	v_add_u32_e32 v5, 63, v5
	v_cndmask_b32_e32 v4, -1, v215, vcc
	v_bitop3_b32 v4, v4, s0, v9 bitop3:0x48
	v_sub_u32_e32 v4, v4, v3
	v_cmp_lt_i32_e32 vcc, -1, v24
	v_add_u32_e32 v12, 63, v4
	v_add_u32_e32 v6, 63, v6
	v_cndmask_b32_e32 v4, -1, v215, vcc
	v_bitop3_b32 v4, v4, s0, v24 bitop3:0x48
	v_sub_u32_e32 v4, v4, v25
	v_add_u32_e32 v7, 63, v7
	v_add_u32_e32 v8, 63, v8
	v_add_u32_e32 v11, 63, v11
	v_add_u32_e32 v4, 63, v4
	s_mov_b32 s0, 31
	v_mov_b32_e32 v9, 0
	s_mov_b64 s[100:101], 0
	s_cmp_lt_i32 s2, 16
	s_cbranch_scc1 .Lradix_done
